# fp8 GEMM MFMAs issued as the plain f8f6f4 form (e4m3 x e4m3, no scale prefix) instead of the MX-scaled form with unit scales: same products, 8-byte instead of 16-byte encoding
# speedup vs baseline: 1.0169x; 1.0102x over previous
.LBB0_235:
	s_add_u32 s4, s0, 0xfffe0080
	s_addc_u32 s5, s1, -1
	s_add_i32 s52, 0, 0x10000
	s_cmp_eq_u32 s51, 4
	s_cselect_b32 s7, s21, s5
	s_cselect_b32 s6, s29, s4
	s_cselect_b32 s5, s23, s50
	s_cselect_b32 s4, s48, s49
	s_add_i32 s53, 0, 0x14000
	ds_read_b128 v[20:23], v192
	ds_read_b128 v[24:27], v249
	ds_read_b128 v[28:31], v192 offset:2048
	ds_read_b128 v[32:35], v249 offset:2048
	ds_read_b128 v[4:7], v192 offset:16384
	ds_read_b128 v[8:11], v249 offset:16384
	ds_read_b128 v[12:15], v192 offset:18432
	ds_read_b128 v[16:19], v249 offset:18432
	v_lshl_add_u64 v[234:235], s[0:1], 0, v[180:181]
	s_add_i32 m0, s37, 0xc000
	ds_read_b128 v[184:187], v193
	ds_read_b128 v[188:191], v250
	ds_read_b128 v[194:197], v193 offset:2048
	ds_read_b128 v[198:201], v250 offset:2048
	ds_read_b128 v[202:205], v193 offset:4096
	ds_read_b128 v[206:209], v250 offset:4096
	ds_read_b128 v[226:229], v193 offset:6144
	ds_read_b128 v[230:233], v250 offset:6144
	global_load_lds_dwordx4 v[234:235], off
	v_lshl_add_u64 v[234:235], s[0:1], 0, v[182:183]
	s_add_i32 m0, s37, 0xe000
	s_nop 0
	global_load_lds_dwordx4 v[234:235], off
	s_waitcnt vmcnt(8)
	s_waitcnt lgkmcnt(0)
	s_barrier
	s_setprio 1
	s_waitcnt lgkmcnt(0)
	v_mfma_f32_16x16x128_f8f6f4 v[96:99], v[20:27], v[184:191], v[96:99]
	v_mfma_f32_16x16x128_f8f6f4 v[92:95], v[28:35], v[184:191], v[92:95]
	v_mfma_f32_16x16x128_f8f6f4 v[88:91], v[20:27], v[194:201], v[88:91]
	v_mfma_f32_16x16x128_f8f6f4 v[84:87], v[28:35], v[194:201], v[84:87]
	v_mfma_f32_16x16x128_f8f6f4 v[80:83], v[20:27], v[202:209], v[80:83]
	v_mfma_f32_16x16x128_f8f6f4 v[76:79], v[28:35], v[202:209], v[76:79]
	v_mfma_f32_16x16x128_f8f6f4 v[72:75], v[20:27], v[226:233], v[72:75]
	v_mfma_f32_16x16x128_f8f6f4 v[68:71], v[28:35], v[226:233], v[68:71]
	s_setprio 0
	s_setprio 1
	v_mfma_f32_16x16x128_f8f6f4 v[160:163], v[4:11], v[184:191], v[160:163]
	v_mfma_f32_16x16x128_f8f6f4 v[156:159], v[12:19], v[184:191], v[156:159]
	v_mfma_f32_16x16x128_f8f6f4 v[152:155], v[4:11], v[194:201], v[152:155]
	v_mfma_f32_16x16x128_f8f6f4 v[148:151], v[12:19], v[194:201], v[148:151]
	v_mfma_f32_16x16x128_f8f6f4 v[144:147], v[4:11], v[202:209], v[144:147]
	v_mfma_f32_16x16x128_f8f6f4 v[140:143], v[12:19], v[202:209], v[140:143]
	v_mfma_f32_16x16x128_f8f6f4 v[136:139], v[4:11], v[226:233], v[136:139]
	v_mfma_f32_16x16x128_f8f6f4 v[132:135], v[12:19], v[226:233], v[132:135]
	s_setprio 0
	s_barrier
	s_add_i32 s52, s52, s36
	v_lshl_add_u64 v[184:185], s[4:5], 0, v[176:177]
	s_mov_b32 m0, s52
	ds_read_b128 v[194:197], v193 offset:16384
	ds_read_b128 v[198:201], v250 offset:16384
	ds_read_b128 v[202:205], v193 offset:18432
	ds_read_b128 v[206:209], v250 offset:18432
	ds_read_b128 v[226:229], v193 offset:20480
	ds_read_b128 v[230:233], v250 offset:20480
	ds_read_b128 v[234:237], v193 offset:22528
	ds_read_b128 v[238:241], v250 offset:22528
	global_load_lds_dwordx4 v[184:185], off
	s_add_i32 m0, s52, 0x2000
	s_add_u32 s54, s4, 0x20000
	v_lshl_add_u64 v[186:187], s[4:5], 0, v[172:173]
	s_addc_u32 s55, s5, 0
	s_add_i32 s52, s53, s36
	global_load_lds_dwordx4 v[186:187], off
	v_lshl_add_u64 v[188:189], s[54:55], 0, v[176:177]
	s_mov_b32 m0, s52
	v_lshl_add_u64 v[190:191], s[6:7], 0, v[174:175]
	global_load_lds_dwordx4 v[188:189], off
	v_lshl_add_u64 v[188:189], s[54:55], 0, v[172:173]
	s_add_i32 m0, s52, 0x2000
	s_nop 0
	global_load_lds_dwordx4 v[188:189], off
	v_lshl_add_u64 v[188:189], s[6:7], 0, v[178:179]
	s_mov_b32 m0, s37
	s_nop 0
	global_load_lds_dwordx4 v[188:189], off
	s_mov_b32 m0, s38
	s_nop 0
	global_load_lds_dwordx4 v[190:191], off
	s_waitcnt vmcnt(8)
	s_waitcnt lgkmcnt(0)
	s_barrier
	s_setprio 1
	s_waitcnt lgkmcnt(0)
	v_mfma_f32_16x16x128_f8f6f4 v[64:67], v[20:27], v[194:201], v[64:67]
	v_mfma_f32_16x16x128_f8f6f4 v[60:63], v[28:35], v[194:201], v[60:63]
	v_mfma_f32_16x16x128_f8f6f4 v[56:59], v[20:27], v[202:209], v[56:59]
	v_mfma_f32_16x16x128_f8f6f4 v[52:55], v[28:35], v[202:209], v[52:55]
	v_mfma_f32_16x16x128_f8f6f4 v[48:51], v[20:27], v[226:233], v[48:51]
	v_mfma_f32_16x16x128_f8f6f4 v[44:47], v[28:35], v[226:233], v[44:47]
	v_mfma_f32_16x16x128_f8f6f4 v[40:43], v[20:27], v[234:241], v[40:43]
	v_mfma_f32_16x16x128_f8f6f4 v[36:39], v[28:35], v[234:241], v[36:39]
	s_setprio 0
	s_setprio 1
	v_mfma_f32_16x16x128_f8f6f4 v[128:131], v[4:11], v[194:201], v[128:131]
	v_mfma_f32_16x16x128_f8f6f4 v[124:127], v[12:19], v[194:201], v[124:127]
	v_mfma_f32_16x16x128_f8f6f4 v[120:123], v[4:11], v[202:209], v[120:123]
	v_mfma_f32_16x16x128_f8f6f4 v[116:119], v[12:19], v[202:209], v[116:119]
	v_mfma_f32_16x16x128_f8f6f4 v[112:115], v[4:11], v[226:233], v[112:115]
	v_mfma_f32_16x16x128_f8f6f4 v[108:111], v[12:19], v[226:233], v[108:111]
	v_mfma_f32_16x16x128_f8f6f4 v[104:107], v[4:11], v[234:241], v[104:107]
	v_mfma_f32_16x16x128_f8f6f4 v[100:103], v[12:19], v[234:241], v[100:103]
	s_setprio 0
	s_barrier
	s_add_i32 s52, 0, 0x18000
	s_add_i32 s53, 0, 0x1c000
	ds_read_b128 v[4:7], v192 offset:32768
	ds_read_b128 v[8:11], v249 offset:32768
	ds_read_b128 v[12:15], v192 offset:34816
	ds_read_b128 v[16:19], v249 offset:34816
	ds_read_b128 v[20:23], v192 offset:49152
	ds_read_b128 v[24:27], v249 offset:49152
	ds_read_b128 v[28:31], v192 offset:51200
	ds_read_b128 v[32:35], v249 offset:51200
	s_add_u32 s6, s6, 0x20000
	s_addc_u32 s7, s7, 0
	s_mov_b32 m0, s39
	v_lshl_add_u64 v[242:243], s[6:7], 0, v[178:179]
	ds_read_b128 v[194:197], v193 offset:32768
	ds_read_b128 v[198:201], v250 offset:32768
	ds_read_b128 v[202:205], v193 offset:34816
	ds_read_b128 v[206:209], v250 offset:34816
	ds_read_b128 v[226:229], v193 offset:36864
	ds_read_b128 v[230:233], v250 offset:36864
	ds_read_b128 v[234:237], v193 offset:38912
	ds_read_b128 v[238:241], v250 offset:38912
	global_load_lds_dwordx4 v[242:243], off
	v_lshl_add_u64 v[242:243], s[6:7], 0, v[174:175]
	s_mov_b32 m0, s42
	s_nop 0
	global_load_lds_dwordx4 v[242:243], off
	s_waitcnt vmcnt(8)
	s_waitcnt lgkmcnt(0)
	s_barrier
	s_setprio 1
	s_waitcnt lgkmcnt(0)
	v_mfma_f32_16x16x128_f8f6f4 v[96:99], v[4:11], v[194:201], v[96:99]
	v_mfma_f32_16x16x128_f8f6f4 v[92:95], v[12:19], v[194:201], v[92:95]
	v_mfma_f32_16x16x128_f8f6f4 v[88:91], v[4:11], v[202:209], v[88:91]
	v_mfma_f32_16x16x128_f8f6f4 v[84:87], v[12:19], v[202:209], v[84:87]
	v_mfma_f32_16x16x128_f8f6f4 v[80:83], v[4:11], v[226:233], v[80:83]
	v_mfma_f32_16x16x128_f8f6f4 v[76:79], v[12:19], v[226:233], v[76:79]
	v_mfma_f32_16x16x128_f8f6f4 v[72:75], v[4:11], v[234:241], v[72:75]
	v_mfma_f32_16x16x128_f8f6f4 v[68:71], v[12:19], v[234:241], v[68:71]
	s_setprio 0
	s_setprio 1
	v_mfma_f32_16x16x128_f8f6f4 v[160:163], v[20:27], v[194:201], v[160:163]
	v_mfma_f32_16x16x128_f8f6f4 v[156:159], v[28:35], v[194:201], v[156:159]
	v_mfma_f32_16x16x128_f8f6f4 v[152:155], v[20:27], v[202:209], v[152:155]
	v_mfma_f32_16x16x128_f8f6f4 v[148:151], v[28:35], v[202:209], v[148:151]
	v_mfma_f32_16x16x128_f8f6f4 v[144:147], v[20:27], v[226:233], v[144:147]
	v_mfma_f32_16x16x128_f8f6f4 v[140:143], v[28:35], v[226:233], v[140:143]
	v_mfma_f32_16x16x128_f8f6f4 v[136:139], v[20:27], v[234:241], v[136:139]
	v_mfma_f32_16x16x128_f8f6f4 v[132:135], v[28:35], v[234:241], v[132:135]
	s_setprio 0
	s_barrier
	s_add_i32 s6, s52, s36
	v_lshl_add_u64 v[184:185], v[184:185], 0, s[56:57]
	s_mov_b32 m0, s6
	ds_read_b128 v[194:197], v193 offset:49152
	ds_read_b128 v[198:201], v250 offset:49152
	ds_read_b128 v[202:205], v193 offset:51200
	ds_read_b128 v[206:209], v250 offset:51200
	ds_read_b128 v[226:229], v193 offset:53248
	ds_read_b128 v[230:233], v250 offset:53248
	ds_read_b128 v[234:237], v193 offset:55296
	ds_read_b128 v[238:241], v250 offset:55296
	global_load_lds_dwordx4 v[184:185], off
	s_add_i32 m0, s6, 0x2000
	s_add_u32 s4, s4, 0x20080
	v_lshl_add_u64 v[184:185], v[186:187], 0, s[56:57]
	s_addc_u32 s5, s5, 0
	s_add_i32 s6, s53, s36
	global_load_lds_dwordx4 v[184:185], off
	v_lshl_add_u64 v[184:185], s[4:5], 0, v[176:177]
	s_mov_b32 m0, s6
	s_nop 0
	global_load_lds_dwordx4 v[184:185], off
	v_lshl_add_u64 v[184:185], s[4:5], 0, v[172:173]
	s_add_i32 m0, s6, 0x2000
	s_nop 0
	global_load_lds_dwordx4 v[184:185], off
	v_lshl_add_u64 v[184:185], v[188:189], 0, s[56:57]
	s_mov_b32 m0, s45
	s_nop 0
	global_load_lds_dwordx4 v[184:185], off
	v_lshl_add_u64 v[184:185], v[190:191], 0, s[56:57]
	s_mov_b32 m0, s46
	s_nop 0
	global_load_lds_dwordx4 v[184:185], off
	s_waitcnt vmcnt(8)
	s_waitcnt lgkmcnt(0)
	s_barrier
	s_setprio 1
	s_waitcnt lgkmcnt(0)
	v_mfma_f32_16x16x128_f8f6f4 v[64:67], v[4:11], v[194:201], v[64:67]
	v_mfma_f32_16x16x128_f8f6f4 v[60:63], v[12:19], v[194:201], v[60:63]
	v_mfma_f32_16x16x128_f8f6f4 v[56:59], v[4:11], v[202:209], v[56:59]
	v_mfma_f32_16x16x128_f8f6f4 v[52:55], v[12:19], v[202:209], v[52:55]
	v_mfma_f32_16x16x128_f8f6f4 v[48:51], v[4:11], v[226:233], v[48:51]
	v_mfma_f32_16x16x128_f8f6f4 v[44:47], v[12:19], v[226:233], v[44:47]
	v_mfma_f32_16x16x128_f8f6f4 v[40:43], v[4:11], v[234:241], v[40:43]
	v_mfma_f32_16x16x128_f8f6f4 v[36:39], v[12:19], v[234:241], v[36:39]
	s_setprio 0
	s_setprio 1
	v_mfma_f32_16x16x128_f8f6f4 v[128:131], v[20:27], v[194:201], v[128:131]
	v_mfma_f32_16x16x128_f8f6f4 v[124:127], v[28:35], v[194:201], v[124:127]
	v_mfma_f32_16x16x128_f8f6f4 v[120:123], v[20:27], v[202:209], v[120:123]
	v_mfma_f32_16x16x128_f8f6f4 v[116:119], v[28:35], v[202:209], v[116:119]
	v_mfma_f32_16x16x128_f8f6f4 v[112:115], v[20:27], v[226:233], v[112:115]
	v_mfma_f32_16x16x128_f8f6f4 v[108:111], v[28:35], v[226:233], v[108:111]
	v_mfma_f32_16x16x128_f8f6f4 v[104:107], v[20:27], v[234:241], v[104:107]
	v_mfma_f32_16x16x128_f8f6f4 v[100:103], v[28:35], v[234:241], v[100:103]
	s_setprio 0
	s_barrier
	s_add_i32 s51, s51, 2
	s_add_u32 s0, s0, 0x100
	s_addc_u32 s1, s1, 0
	s_add_u32 s49, s49, 0x100
	s_addc_u32 s50, s50, 0
	s_cmp_gt_u32 s51, 5
	s_cbranch_scc0 .LBB0_235
	s_and_b64 vcc, exec, s[18:19]
	s_cbranch_vccz .LBB0_238
	s_barrier

.LBB0_623:
	s_add_i32 s64, 0, 0x10000
	s_add_i32 s65, 0, 0x14000
	ds_read_b128 v[4:7], v189
	ds_read_b128 v[8:11], v245
	ds_read_b128 v[12:15], v189 offset:2048
	ds_read_b128 v[16:19], v245 offset:2048
	ds_read_b128 v[20:23], v189 offset:16384
	ds_read_b128 v[24:27], v245 offset:16384
	ds_read_b128 v[28:31], v189 offset:18432
	ds_read_b128 v[32:35], v245 offset:18432
	s_add_u32 s34, s34, 0x10000
	s_addc_u32 s35, s35, 0
	v_lshl_add_u64 v[164:165], s[34:35], 0, v[178:179]
	s_add_i32 m0, s43, 0xc000
	ds_read_b128 v[180:183], v190
	ds_read_b128 v[184:187], v246
	ds_read_b128 v[192:195], v190 offset:2048
	ds_read_b128 v[196:199], v246 offset:2048
	ds_read_b128 v[200:203], v190 offset:4096
	ds_read_b128 v[204:207], v246 offset:4096
	ds_read_b128 v[226:229], v190 offset:6144
	ds_read_b128 v[230:233], v246 offset:6144
	global_load_lds_dwordx4 v[164:165], off
	v_lshl_add_u64 v[164:165], s[34:35], 0, v[174:175]
	s_add_i32 m0, s43, 0xe000
	s_nop 0
	global_load_lds_dwordx4 v[164:165], off
	s_waitcnt vmcnt(8)
	s_waitcnt lgkmcnt(0)
	s_barrier
	s_setprio 1
	s_waitcnt lgkmcnt(0)
	v_mfma_f32_16x16x128_f8f6f4 v[160:163], v[4:11], v[180:187], v[160:163]
	v_mfma_f32_16x16x128_f8f6f4 v[156:159], v[12:19], v[180:187], v[156:159]
	v_mfma_f32_16x16x128_f8f6f4 v[144:147], v[4:11], v[192:199], v[144:147]
	v_mfma_f32_16x16x128_f8f6f4 v[140:143], v[12:19], v[192:199], v[140:143]
	v_mfma_f32_16x16x128_f8f6f4 v[128:131], v[4:11], v[200:207], v[128:131]
	v_mfma_f32_16x16x128_f8f6f4 v[124:127], v[12:19], v[200:207], v[124:127]
	v_mfma_f32_16x16x128_f8f6f4 v[112:115], v[4:11], v[226:233], v[112:115]
	v_mfma_f32_16x16x128_f8f6f4 v[108:111], v[12:19], v[226:233], v[108:111]
	s_setprio 0
	s_setprio 1
	v_mfma_f32_16x16x128_f8f6f4 v[152:155], v[20:27], v[180:187], v[152:155]
	v_mfma_f32_16x16x128_f8f6f4 v[148:151], v[28:35], v[180:187], v[148:151]
	v_mfma_f32_16x16x128_f8f6f4 v[136:139], v[20:27], v[192:199], v[136:139]
	v_mfma_f32_16x16x128_f8f6f4 v[132:135], v[28:35], v[192:199], v[132:135]
	v_mfma_f32_16x16x128_f8f6f4 v[120:123], v[20:27], v[200:207], v[120:123]
	v_mfma_f32_16x16x128_f8f6f4 v[116:119], v[28:35], v[200:207], v[116:119]
	v_mfma_f32_16x16x128_f8f6f4 v[104:107], v[20:27], v[226:233], v[104:107]
	v_mfma_f32_16x16x128_f8f6f4 v[100:103], v[28:35], v[226:233], v[100:103]
	s_setprio 0
	s_barrier
	s_add_i32 s34, s64, s42
	v_lshl_add_u64 v[182:183], s[36:37], 0, v[176:177]
	s_mov_b32 m0, s34
	ds_read_b128 v[192:195], v190 offset:16384
	ds_read_b128 v[196:199], v246 offset:16384
	ds_read_b128 v[200:203], v190 offset:18432
	ds_read_b128 v[204:207], v246 offset:18432
	ds_read_b128 v[226:229], v190 offset:20480
	ds_read_b128 v[230:233], v246 offset:20480
	ds_read_b128 v[234:237], v190 offset:22528
	ds_read_b128 v[238:241], v246 offset:22528
	global_load_lds_dwordx4 v[182:183], off
	s_add_i32 m0, s34, 0x2000
	s_add_u32 s34, s36, 0x10000
	v_lshl_add_u64 v[184:185], s[36:37], 0, v[172:173]
	s_addc_u32 s35, s37, 0
	s_add_i32 s64, s65, s42
	global_load_lds_dwordx4 v[184:185], off
	v_lshl_add_u64 v[164:165], s[34:35], 0, v[176:177]
	s_mov_b32 m0, s64
	v_lshl_add_u64 v[186:187], s[30:31], 0, v[178:179]
	global_load_lds_dwordx4 v[164:165], off
	v_lshl_add_u64 v[164:165], s[34:35], 0, v[172:173]
	s_add_i32 m0, s64, 0x2000
	v_lshl_add_u64 v[180:181], s[30:31], 0, v[174:175]
	global_load_lds_dwordx4 v[164:165], off
	s_mov_b32 m0, s43
	s_nop 0
	global_load_lds_dwordx4 v[186:187], off
	s_mov_b32 m0, s44
	s_nop 0
	global_load_lds_dwordx4 v[180:181], off
	s_waitcnt vmcnt(8)
	s_waitcnt lgkmcnt(0)
	s_barrier
	s_setprio 1
	s_waitcnt lgkmcnt(0)
	v_mfma_f32_16x16x128_f8f6f4 v[96:99], v[4:11], v[192:199], v[96:99]
	v_mfma_f32_16x16x128_f8f6f4 v[92:95], v[12:19], v[192:199], v[92:95]
	v_mfma_f32_16x16x128_f8f6f4 v[80:83], v[4:11], v[200:207], v[80:83]
	v_mfma_f32_16x16x128_f8f6f4 v[76:79], v[12:19], v[200:207], v[76:79]
	v_mfma_f32_16x16x128_f8f6f4 v[64:67], v[4:11], v[226:233], v[64:67]
	v_mfma_f32_16x16x128_f8f6f4 v[60:63], v[12:19], v[226:233], v[60:63]
	v_mfma_f32_16x16x128_f8f6f4 v[48:51], v[4:11], v[234:241], v[48:51]
	v_mfma_f32_16x16x128_f8f6f4 v[44:47], v[12:19], v[234:241], v[44:47]
	s_setprio 0
	s_setprio 1
	v_mfma_f32_16x16x128_f8f6f4 v[88:91], v[20:27], v[192:199], v[88:91]
	v_mfma_f32_16x16x128_f8f6f4 v[84:87], v[28:35], v[192:199], v[84:87]
	v_mfma_f32_16x16x128_f8f6f4 v[72:75], v[20:27], v[200:207], v[72:75]
	v_mfma_f32_16x16x128_f8f6f4 v[68:71], v[28:35], v[200:207], v[68:71]
	v_mfma_f32_16x16x128_f8f6f4 v[56:59], v[20:27], v[226:233], v[56:59]
	v_mfma_f32_16x16x128_f8f6f4 v[52:55], v[28:35], v[226:233], v[52:55]
	v_mfma_f32_16x16x128_f8f6f4 v[40:43], v[20:27], v[234:241], v[40:43]
	v_mfma_f32_16x16x128_f8f6f4 v[36:39], v[28:35], v[234:241], v[36:39]
	s_setprio 0
	s_barrier
	s_add_i32 s34, 0, 0x18000
	s_add_i32 s35, 0, 0x1c000
	ds_read_b128 v[12:15], v189 offset:32768
	ds_read_b128 v[16:19], v245 offset:32768
	ds_read_b128 v[28:31], v189 offset:34816
	ds_read_b128 v[32:35], v245 offset:34816
	ds_read_b128 v[4:7], v189 offset:49152
	ds_read_b128 v[8:11], v245 offset:49152
	ds_read_b128 v[20:23], v189 offset:51200
	ds_read_b128 v[24:27], v245 offset:51200
	s_add_u32 s30, s30, 0x10000
	s_addc_u32 s31, s31, 0
	s_mov_b32 m0, s45
	v_lshl_add_u64 v[164:165], s[30:31], 0, v[178:179]
	ds_read_b128 v[192:195], v190 offset:32768
	ds_read_b128 v[196:199], v246 offset:32768
	ds_read_b128 v[200:203], v190 offset:34816
	ds_read_b128 v[204:207], v246 offset:34816
	ds_read_b128 v[226:229], v190 offset:36864
	ds_read_b128 v[230:233], v246 offset:36864
	ds_read_b128 v[234:237], v190 offset:38912
	ds_read_b128 v[238:241], v246 offset:38912
	global_load_lds_dwordx4 v[164:165], off
	v_lshl_add_u64 v[164:165], s[30:31], 0, v[174:175]
	s_mov_b32 m0, s46
	s_nop 0
	global_load_lds_dwordx4 v[164:165], off
	s_waitcnt vmcnt(8)
	s_waitcnt lgkmcnt(0)
	s_barrier
	s_setprio 1
	s_waitcnt lgkmcnt(0)
	v_mfma_f32_16x16x128_f8f6f4 v[160:163], v[12:19], v[192:199], v[160:163]
	v_mfma_f32_16x16x128_f8f6f4 v[156:159], v[28:35], v[192:199], v[156:159]
	v_mfma_f32_16x16x128_f8f6f4 v[144:147], v[12:19], v[200:207], v[144:147]
	v_mfma_f32_16x16x128_f8f6f4 v[140:143], v[28:35], v[200:207], v[140:143]
	v_mfma_f32_16x16x128_f8f6f4 v[128:131], v[12:19], v[226:233], v[128:131]
	v_mfma_f32_16x16x128_f8f6f4 v[124:127], v[28:35], v[226:233], v[124:127]
	v_mfma_f32_16x16x128_f8f6f4 v[112:115], v[12:19], v[234:241], v[112:115]
	v_mfma_f32_16x16x128_f8f6f4 v[108:111], v[28:35], v[234:241], v[108:111]
	s_setprio 0
	s_setprio 1
	v_mfma_f32_16x16x128_f8f6f4 v[152:155], v[4:11], v[192:199], v[152:155]
	v_mfma_f32_16x16x128_f8f6f4 v[148:151], v[20:27], v[192:199], v[148:151]
	v_mfma_f32_16x16x128_f8f6f4 v[136:139], v[4:11], v[200:207], v[136:139]
	v_mfma_f32_16x16x128_f8f6f4 v[132:135], v[20:27], v[200:207], v[132:135]
	v_mfma_f32_16x16x128_f8f6f4 v[120:123], v[4:11], v[226:233], v[120:123]
	v_mfma_f32_16x16x128_f8f6f4 v[116:119], v[20:27], v[226:233], v[116:119]
	v_mfma_f32_16x16x128_f8f6f4 v[104:107], v[4:11], v[234:241], v[104:107]
	v_mfma_f32_16x16x128_f8f6f4 v[100:103], v[20:27], v[234:241], v[100:103]
	s_setprio 0
	s_barrier
	s_mov_b64 s[64:65], 0x80
	s_add_i32 s30, s34, s42
	v_lshl_add_u64 v[164:165], v[182:183], 0, s[64:65]
	s_mov_b32 m0, s30
	ds_read_b128 v[192:195], v190 offset:49152
	ds_read_b128 v[196:199], v246 offset:49152
	ds_read_b128 v[200:203], v190 offset:51200
	ds_read_b128 v[204:207], v246 offset:51200
	ds_read_b128 v[226:229], v190 offset:53248
	ds_read_b128 v[230:233], v246 offset:53248
	ds_read_b128 v[234:237], v190 offset:55296
	ds_read_b128 v[238:241], v246 offset:55296
	global_load_lds_dwordx4 v[164:165], off
	s_add_i32 m0, s30, 0x2000
	s_add_u32 s30, s36, 0x10080
	v_lshl_add_u64 v[164:165], v[184:185], 0, s[64:65]
	s_addc_u32 s31, s37, 0
	s_add_i32 s34, s35, s42
	global_load_lds_dwordx4 v[164:165], off
	v_lshl_add_u64 v[164:165], s[30:31], 0, v[176:177]
	s_mov_b32 m0, s34
	s_nop 0
	global_load_lds_dwordx4 v[164:165], off
	v_lshl_add_u64 v[164:165], s[30:31], 0, v[172:173]
	s_add_i32 m0, s34, 0x2000
	s_nop 0
	global_load_lds_dwordx4 v[164:165], off
	v_lshl_add_u64 v[164:165], v[186:187], 0, s[64:65]
	s_mov_b32 m0, s53
	s_nop 0
	global_load_lds_dwordx4 v[164:165], off
	v_lshl_add_u64 v[164:165], v[180:181], 0, s[64:65]
	s_mov_b32 m0, s54
	s_nop 0
	global_load_lds_dwordx4 v[164:165], off
	s_waitcnt vmcnt(8)
	s_waitcnt lgkmcnt(0)
	s_barrier
	s_setprio 1
	s_waitcnt lgkmcnt(0)
	v_mfma_f32_16x16x128_f8f6f4 v[96:99], v[12:19], v[192:199], v[96:99]
	v_mfma_f32_16x16x128_f8f6f4 v[92:95], v[28:35], v[192:199], v[92:95]
	v_mfma_f32_16x16x128_f8f6f4 v[80:83], v[12:19], v[200:207], v[80:83]
	v_mfma_f32_16x16x128_f8f6f4 v[76:79], v[28:35], v[200:207], v[76:79]
	v_mfma_f32_16x16x128_f8f6f4 v[64:67], v[12:19], v[226:233], v[64:67]
	v_mfma_f32_16x16x128_f8f6f4 v[60:63], v[28:35], v[226:233], v[60:63]
	v_mfma_f32_16x16x128_f8f6f4 v[48:51], v[12:19], v[234:241], v[48:51]
	v_mfma_f32_16x16x128_f8f6f4 v[44:47], v[28:35], v[234:241], v[44:47]
	s_setprio 0
	s_setprio 1
	v_mfma_f32_16x16x128_f8f6f4 v[88:91], v[4:11], v[192:199], v[88:91]
	v_mfma_f32_16x16x128_f8f6f4 v[84:87], v[20:27], v[192:199], v[84:87]
	v_mfma_f32_16x16x128_f8f6f4 v[72:75], v[4:11], v[200:207], v[72:75]
	v_mfma_f32_16x16x128_f8f6f4 v[68:71], v[20:27], v[200:207], v[68:71]
	v_mfma_f32_16x16x128_f8f6f4 v[56:59], v[4:11], v[226:233], v[56:59]
	v_mfma_f32_16x16x128_f8f6f4 v[52:55], v[20:27], v[226:233], v[52:55]
	v_mfma_f32_16x16x128_f8f6f4 v[40:43], v[4:11], v[234:241], v[40:43]
	v_mfma_f32_16x16x128_f8f6f4 v[36:39], v[20:27], v[234:241], v[36:39]
	s_setprio 0
	s_barrier
	s_mov_b64 s[64:65], s[72:73]
	s_add_i32 s64, s64, 2
	s_add_u32 s28, s28, 0x100
	s_addc_u32 s29, s29, 0
	s_cmp_gt_u32 s63, 5
	s_cbranch_scc1 .LBB0_632

.LBB0_702:
	s_add_u32 s18, s0, 0xffed0080
	s_addc_u32 s19, s1, -1
	s_add_i32 s47, 0, 0x10000
	s_cmp_eq_u32 s46, 4
	s_cselect_b32 s21, s15, s19
	s_cselect_b32 s20, s14, s18
	s_cselect_b32 s19, s13, s45
	s_cselect_b32 s18, s43, s44
	s_add_i32 s48, 0, 0x14000
	ds_read_b128 v[20:23], v226
	ds_read_b128 v[24:27], v245
	ds_read_b128 v[28:31], v226 offset:2048
	ds_read_b128 v[32:35], v245 offset:2048
	ds_read_b128 v[4:7], v226 offset:16384
	ds_read_b128 v[8:11], v245 offset:16384
	ds_read_b128 v[12:15], v226 offset:18432
	ds_read_b128 v[16:19], v245 offset:18432
	v_lshl_add_u64 v[164:165], s[0:1], 0, v[180:181]
	s_add_i32 m0, s27, 0xc000
	ds_read_b128 v[184:187], v227
	ds_read_b128 v[188:191], v246
	ds_read_b128 v[192:195], v227 offset:2048
	ds_read_b128 v[196:199], v246 offset:2048
	ds_read_b128 v[200:203], v227 offset:4096
	ds_read_b128 v[204:207], v246 offset:4096
	ds_read_b128 v[228:231], v227 offset:6144
	ds_read_b128 v[232:235], v246 offset:6144
	global_load_lds_dwordx4 v[164:165], off
	v_lshl_add_u64 v[164:165], s[0:1], 0, v[182:183]
	s_add_i32 m0, s27, 0xe000
	s_nop 0
	global_load_lds_dwordx4 v[164:165], off
	s_waitcnt vmcnt(8)
	s_waitcnt lgkmcnt(0)
	s_barrier
	s_setprio 1
	s_waitcnt lgkmcnt(0)
	v_mfma_f32_16x16x128_f8f6f4 v[160:163], v[20:27], v[184:191], v[160:163]
	v_mfma_f32_16x16x128_f8f6f4 v[156:159], v[28:35], v[184:191], v[156:159]
	v_mfma_f32_16x16x128_f8f6f4 v[144:147], v[20:27], v[192:199], v[144:147]
	v_mfma_f32_16x16x128_f8f6f4 v[140:143], v[28:35], v[192:199], v[140:143]
	v_mfma_f32_16x16x128_f8f6f4 v[128:131], v[20:27], v[200:207], v[128:131]
	v_mfma_f32_16x16x128_f8f6f4 v[124:127], v[28:35], v[200:207], v[124:127]
	v_mfma_f32_16x16x128_f8f6f4 v[112:115], v[20:27], v[228:235], v[112:115]
	v_mfma_f32_16x16x128_f8f6f4 v[108:111], v[28:35], v[228:235], v[108:111]
	s_setprio 0
	s_setprio 1
	v_mfma_f32_16x16x128_f8f6f4 v[152:155], v[4:11], v[184:191], v[152:155]
	v_mfma_f32_16x16x128_f8f6f4 v[148:151], v[12:19], v[184:191], v[148:151]
	v_mfma_f32_16x16x128_f8f6f4 v[136:139], v[4:11], v[192:199], v[136:139]
	v_mfma_f32_16x16x128_f8f6f4 v[132:135], v[12:19], v[192:199], v[132:135]
	v_mfma_f32_16x16x128_f8f6f4 v[120:123], v[4:11], v[200:207], v[120:123]
	v_mfma_f32_16x16x128_f8f6f4 v[116:119], v[12:19], v[200:207], v[116:119]
	v_mfma_f32_16x16x128_f8f6f4 v[104:107], v[4:11], v[228:235], v[104:107]
	v_mfma_f32_16x16x128_f8f6f4 v[100:103], v[12:19], v[228:235], v[100:103]
	s_setprio 0
	s_barrier
	s_add_i32 s47, s47, s26
	v_lshl_add_u64 v[184:185], s[18:19], 0, v[176:177]
	s_mov_b32 m0, s47
	ds_read_b128 v[192:195], v227 offset:16384
	ds_read_b128 v[196:199], v246 offset:16384
	ds_read_b128 v[200:203], v227 offset:18432
	ds_read_b128 v[204:207], v246 offset:18432
	ds_read_b128 v[228:231], v227 offset:20480
	ds_read_b128 v[232:235], v246 offset:20480
	ds_read_b128 v[236:239], v227 offset:22528
	ds_read_b128 v[240:243], v246 offset:22528
	global_load_lds_dwordx4 v[184:185], off
	s_add_i32 m0, s47, 0x2000
	s_add_u32 s50, s18, 0x20000
	v_lshl_add_u64 v[186:187], s[18:19], 0, v[172:173]
	s_addc_u32 s51, s19, 0
	s_add_i32 s47, s48, s26
	global_load_lds_dwordx4 v[186:187], off
	v_lshl_add_u64 v[164:165], s[50:51], 0, v[176:177]
	s_mov_b32 m0, s47
	v_lshl_add_u64 v[188:189], s[20:21], 0, v[178:179]
	global_load_lds_dwordx4 v[164:165], off
	v_lshl_add_u64 v[164:165], s[50:51], 0, v[172:173]
	s_add_i32 m0, s47, 0x2000
	v_lshl_add_u64 v[190:191], s[20:21], 0, v[174:175]
	global_load_lds_dwordx4 v[164:165], off
	s_mov_b32 m0, s27
	s_nop 0
	global_load_lds_dwordx4 v[188:189], off
	s_mov_b32 m0, s28
	s_nop 0
	global_load_lds_dwordx4 v[190:191], off
	s_waitcnt vmcnt(8)
	s_waitcnt lgkmcnt(0)
	s_barrier
	s_setprio 1
	s_waitcnt lgkmcnt(0)
	v_mfma_f32_16x16x128_f8f6f4 v[96:99], v[20:27], v[192:199], v[96:99]
	v_mfma_f32_16x16x128_f8f6f4 v[92:95], v[28:35], v[192:199], v[92:95]
	v_mfma_f32_16x16x128_f8f6f4 v[80:83], v[20:27], v[200:207], v[80:83]
	v_mfma_f32_16x16x128_f8f6f4 v[76:79], v[28:35], v[200:207], v[76:79]
	v_mfma_f32_16x16x128_f8f6f4 v[64:67], v[20:27], v[228:235], v[64:67]
	v_mfma_f32_16x16x128_f8f6f4 v[60:63], v[28:35], v[228:235], v[60:63]
	v_mfma_f32_16x16x128_f8f6f4 v[48:51], v[20:27], v[236:243], v[48:51]
	v_mfma_f32_16x16x128_f8f6f4 v[44:47], v[28:35], v[236:243], v[44:47]
	s_setprio 0
	s_setprio 1
	v_mfma_f32_16x16x128_f8f6f4 v[88:91], v[4:11], v[192:199], v[88:91]
	v_mfma_f32_16x16x128_f8f6f4 v[84:87], v[12:19], v[192:199], v[84:87]
	v_mfma_f32_16x16x128_f8f6f4 v[72:75], v[4:11], v[200:207], v[72:75]
	v_mfma_f32_16x16x128_f8f6f4 v[68:71], v[12:19], v[200:207], v[68:71]
	v_mfma_f32_16x16x128_f8f6f4 v[56:59], v[4:11], v[228:235], v[56:59]
	v_mfma_f32_16x16x128_f8f6f4 v[52:55], v[12:19], v[228:235], v[52:55]
	v_mfma_f32_16x16x128_f8f6f4 v[40:43], v[4:11], v[236:243], v[40:43]
	v_mfma_f32_16x16x128_f8f6f4 v[36:39], v[12:19], v[236:243], v[36:39]
	s_setprio 0
	s_barrier
	s_add_i32 s47, 0, 0x18000
	s_add_i32 s48, 0, 0x1c000
	ds_read_b128 v[4:7], v226 offset:32768
	ds_read_b128 v[8:11], v245 offset:32768
	ds_read_b128 v[12:15], v226 offset:34816
	ds_read_b128 v[16:19], v245 offset:34816
	ds_read_b128 v[20:23], v226 offset:49152
	ds_read_b128 v[24:27], v245 offset:49152
	ds_read_b128 v[28:31], v226 offset:51200
	ds_read_b128 v[32:35], v245 offset:51200
	s_add_u32 s20, s20, 0x130000
	s_addc_u32 s21, s21, 0
	s_mov_b32 m0, s29
	v_lshl_add_u64 v[164:165], s[20:21], 0, v[178:179]
	ds_read_b128 v[192:195], v227 offset:32768
	ds_read_b128 v[196:199], v246 offset:32768
	ds_read_b128 v[200:203], v227 offset:34816
	ds_read_b128 v[204:207], v246 offset:34816
	ds_read_b128 v[228:231], v227 offset:36864
	ds_read_b128 v[232:235], v246 offset:36864
	ds_read_b128 v[236:239], v227 offset:38912
	ds_read_b128 v[240:243], v246 offset:38912
	global_load_lds_dwordx4 v[164:165], off
	v_lshl_add_u64 v[164:165], s[20:21], 0, v[174:175]
	s_mov_b32 m0, s30
	s_nop 0
	global_load_lds_dwordx4 v[164:165], off
	s_waitcnt vmcnt(8)
	s_waitcnt lgkmcnt(0)
	s_barrier
	s_setprio 1
	s_waitcnt lgkmcnt(0)
	v_mfma_f32_16x16x128_f8f6f4 v[160:163], v[4:11], v[192:199], v[160:163]
	v_mfma_f32_16x16x128_f8f6f4 v[156:159], v[12:19], v[192:199], v[156:159]
	v_mfma_f32_16x16x128_f8f6f4 v[144:147], v[4:11], v[200:207], v[144:147]
	v_mfma_f32_16x16x128_f8f6f4 v[140:143], v[12:19], v[200:207], v[140:143]
	v_mfma_f32_16x16x128_f8f6f4 v[128:131], v[4:11], v[228:235], v[128:131]
	v_mfma_f32_16x16x128_f8f6f4 v[124:127], v[12:19], v[228:235], v[124:127]
	v_mfma_f32_16x16x128_f8f6f4 v[112:115], v[4:11], v[236:243], v[112:115]
	v_mfma_f32_16x16x128_f8f6f4 v[108:111], v[12:19], v[236:243], v[108:111]
	s_setprio 0
	s_setprio 1
	v_mfma_f32_16x16x128_f8f6f4 v[152:155], v[20:27], v[192:199], v[152:155]
	v_mfma_f32_16x16x128_f8f6f4 v[148:151], v[28:35], v[192:199], v[148:151]
	v_mfma_f32_16x16x128_f8f6f4 v[136:139], v[20:27], v[200:207], v[136:139]
	v_mfma_f32_16x16x128_f8f6f4 v[132:135], v[28:35], v[200:207], v[132:135]
	v_mfma_f32_16x16x128_f8f6f4 v[120:123], v[20:27], v[228:235], v[120:123]
	v_mfma_f32_16x16x128_f8f6f4 v[116:119], v[28:35], v[228:235], v[116:119]
	v_mfma_f32_16x16x128_f8f6f4 v[104:107], v[20:27], v[236:243], v[104:107]
	v_mfma_f32_16x16x128_f8f6f4 v[100:103], v[28:35], v[236:243], v[100:103]
	s_setprio 0
	s_barrier
	s_add_i32 s20, s47, s26
	v_lshl_add_u64 v[164:165], v[184:185], 0, s[52:53]
	s_mov_b32 m0, s20
	ds_read_b128 v[192:195], v227 offset:49152
	ds_read_b128 v[196:199], v246 offset:49152
	ds_read_b128 v[200:203], v227 offset:51200
	ds_read_b128 v[204:207], v246 offset:51200
	ds_read_b128 v[228:231], v227 offset:53248
	ds_read_b128 v[232:235], v246 offset:53248
	ds_read_b128 v[236:239], v227 offset:55296
	ds_read_b128 v[240:243], v246 offset:55296
	global_load_lds_dwordx4 v[164:165], off
	s_add_i32 m0, s20, 0x2000
	s_add_u32 s18, s18, 0x20080
	v_lshl_add_u64 v[164:165], v[186:187], 0, s[52:53]
	s_addc_u32 s19, s19, 0
	s_add_i32 s20, s48, s26
	global_load_lds_dwordx4 v[164:165], off
	v_lshl_add_u64 v[164:165], s[18:19], 0, v[176:177]
	s_mov_b32 m0, s20
	s_nop 0
	global_load_lds_dwordx4 v[164:165], off
	v_lshl_add_u64 v[164:165], s[18:19], 0, v[172:173]
	s_add_i32 m0, s20, 0x2000
	s_nop 0
	global_load_lds_dwordx4 v[164:165], off
	v_lshl_add_u64 v[164:165], v[188:189], 0, s[52:53]
	s_mov_b32 m0, s38
	s_nop 0
	global_load_lds_dwordx4 v[164:165], off
	v_lshl_add_u64 v[164:165], v[190:191], 0, s[52:53]
	s_mov_b32 m0, s39
	s_nop 0
	global_load_lds_dwordx4 v[164:165], off
	s_waitcnt vmcnt(8)
	s_waitcnt lgkmcnt(0)
	s_barrier
	s_setprio 1
	s_waitcnt lgkmcnt(0)
	v_mfma_f32_16x16x128_f8f6f4 v[96:99], v[4:11], v[192:199], v[96:99]
	v_mfma_f32_16x16x128_f8f6f4 v[92:95], v[12:19], v[192:199], v[92:95]
	v_mfma_f32_16x16x128_f8f6f4 v[80:83], v[4:11], v[200:207], v[80:83]
	v_mfma_f32_16x16x128_f8f6f4 v[76:79], v[12:19], v[200:207], v[76:79]
	v_mfma_f32_16x16x128_f8f6f4 v[64:67], v[4:11], v[228:235], v[64:67]
	v_mfma_f32_16x16x128_f8f6f4 v[60:63], v[12:19], v[228:235], v[60:63]
	v_mfma_f32_16x16x128_f8f6f4 v[48:51], v[4:11], v[236:243], v[48:51]
	v_mfma_f32_16x16x128_f8f6f4 v[44:47], v[12:19], v[236:243], v[44:47]
	s_setprio 0
	s_setprio 1
	v_mfma_f32_16x16x128_f8f6f4 v[88:91], v[20:27], v[192:199], v[88:91]
	v_mfma_f32_16x16x128_f8f6f4 v[84:87], v[28:35], v[192:199], v[84:87]
	v_mfma_f32_16x16x128_f8f6f4 v[72:75], v[20:27], v[200:207], v[72:75]
	v_mfma_f32_16x16x128_f8f6f4 v[68:71], v[28:35], v[200:207], v[68:71]
	v_mfma_f32_16x16x128_f8f6f4 v[56:59], v[20:27], v[228:235], v[56:59]
	v_mfma_f32_16x16x128_f8f6f4 v[52:55], v[28:35], v[228:235], v[52:55]
	v_mfma_f32_16x16x128_f8f6f4 v[40:43], v[20:27], v[236:243], v[40:43]
	v_mfma_f32_16x16x128_f8f6f4 v[36:39], v[28:35], v[236:243], v[36:39]
	s_setprio 0
	s_barrier
	s_add_i32 s46, s46, 2
	s_add_u32 s0, s0, 0x100
	s_addc_u32 s1, s1, 0
	s_add_u32 s44, s44, 0x100
	s_addc_u32 s45, s45, 0
	s_cmp_gt_u32 s46, 5
	s_cbranch_scc0 .LBB0_702
	s_and_b64 vcc, exec, s[10:11]
	s_cbranch_vccz .LBB0_705
	s_barrier

.LBB0_879:
	s_add_u32 s38, s34, 0x80
	s_addc_u32 s39, s35, 0
	s_add_i32 s66, 0, 0x10000
	s_cmp_eq_u32 s65, 4
	s_cselect_b64 vcc, -1, 0
	s_and_b64 s[36:37], vcc, exec
	s_cselect_b32 s39, s1, s39
	s_cselect_b32 s38, s0, s38
	s_cselect_b32 s37, s29, s64
	s_cselect_b32 s36, s28, s63
	s_add_i32 s67, 0, 0x14000
	ds_read_b128 v[20:23], v192
	ds_read_b128 v[24:27], v207
	ds_read_b128 v[28:31], v192 offset:2048
	ds_read_b128 v[32:35], v207 offset:2048
	ds_read_b128 v[4:7], v192 offset:16384
	ds_read_b128 v[8:11], v207 offset:16384
	ds_read_b128 v[12:15], v192 offset:18432
	ds_read_b128 v[16:19], v207 offset:18432
	v_lshl_add_u64 v[164:165], s[34:35], 0, v[178:179]
	s_add_i32 m0, s47, 0xc000
	ds_read_b128 v[182:185], v193
	ds_read_b128 v[186:189], v208
	ds_read_b128 v[198:201], v193 offset:2048
	ds_read_b128 v[202:205], v208 offset:2048
	ds_read_b128 v[226:229], v193 offset:4096
	ds_read_b128 v[230:233], v208 offset:4096
	ds_read_b128 v[234:237], v193 offset:6144
	ds_read_b128 v[238:241], v208 offset:6144
	global_load_lds_dwordx4 v[164:165], off
	v_lshl_add_u64 v[164:165], s[34:35], 0, v[180:181]
	s_add_i32 m0, s47, 0xe000
	s_nop 0
	global_load_lds_dwordx4 v[164:165], off
	s_waitcnt vmcnt(8)
	s_waitcnt lgkmcnt(0)
	s_barrier
	s_setprio 1
	s_waitcnt lgkmcnt(0)
	v_mfma_f32_16x16x128_f8f6f4 v[160:163], v[20:27], v[182:189], v[160:163]
	v_mfma_f32_16x16x128_f8f6f4 v[156:159], v[28:35], v[182:189], v[156:159]
	v_mfma_f32_16x16x128_f8f6f4 v[144:147], v[20:27], v[198:205], v[144:147]
	v_mfma_f32_16x16x128_f8f6f4 v[140:143], v[28:35], v[198:205], v[140:143]
	v_mfma_f32_16x16x128_f8f6f4 v[128:131], v[20:27], v[226:233], v[128:131]
	v_mfma_f32_16x16x128_f8f6f4 v[124:127], v[28:35], v[226:233], v[124:127]
	v_mfma_f32_16x16x128_f8f6f4 v[112:115], v[20:27], v[234:241], v[112:115]
	v_mfma_f32_16x16x128_f8f6f4 v[108:111], v[28:35], v[234:241], v[108:111]
	s_setprio 0
	s_setprio 1
	v_mfma_f32_16x16x128_f8f6f4 v[152:155], v[4:11], v[182:189], v[152:155]
	v_mfma_f32_16x16x128_f8f6f4 v[148:151], v[12:19], v[182:189], v[148:151]
	v_mfma_f32_16x16x128_f8f6f4 v[136:139], v[4:11], v[198:205], v[136:139]
	v_mfma_f32_16x16x128_f8f6f4 v[132:135], v[12:19], v[198:205], v[132:135]
	v_mfma_f32_16x16x128_f8f6f4 v[120:123], v[4:11], v[226:233], v[120:123]
	v_mfma_f32_16x16x128_f8f6f4 v[116:119], v[12:19], v[226:233], v[116:119]
	v_mfma_f32_16x16x128_f8f6f4 v[104:107], v[4:11], v[234:241], v[104:107]
	v_mfma_f32_16x16x128_f8f6f4 v[100:103], v[12:19], v[234:241], v[100:103]
	s_setprio 0
	s_barrier
	s_add_i32 s66, s66, s46
	v_lshl_add_u64 v[182:183], s[36:37], 0, v[176:177]
	s_mov_b32 m0, s66
	ds_read_b128 v[198:201], v193 offset:16384
	ds_read_b128 v[202:205], v208 offset:16384
	ds_read_b128 v[226:229], v193 offset:18432
	ds_read_b128 v[230:233], v208 offset:18432
	ds_read_b128 v[234:237], v193 offset:20480
	ds_read_b128 v[238:241], v208 offset:20480
	ds_read_b128 v[242:245], v193 offset:22528
	ds_read_b128 v[246:249], v208 offset:22528
	global_load_lds_dwordx4 v[182:183], off
	s_add_i32 m0, s66, 0x2000
	s_add_u32 s68, s36, 0x20000
	v_lshl_add_u64 v[184:185], s[36:37], 0, v[174:175]
	s_addc_u32 s69, s37, 0
	s_add_i32 s66, s67, s46
	global_load_lds_dwordx4 v[184:185], off
	v_lshl_add_u64 v[164:165], s[68:69], 0, v[176:177]
	s_mov_b32 m0, s66
	v_mov_b32_e32 v167, v2
	global_load_lds_dwordx4 v[164:165], off
	v_lshl_add_u64 v[164:165], s[68:69], 0, v[174:175]
	s_add_i32 m0, s66, 0x2000
	s_nop 0
	global_load_lds_dwordx4 v[164:165], off
	v_cndmask_b32_e32 v165, v196, v194, vcc
	v_lshlrev_b32_e32 v164, 10, v165
	v_and_b32_e32 v164, 0x3fffc00, v164
	v_add_u32_e32 v164, v164, v1
	s_mov_b32 m0, s47
	v_bfe_u32 v165, v165, 16, 16
	global_load_lds_dwordx4 v164, s[38:39]
	v_lshl_add_u32 v166, v165, 10, v1
	s_mov_b32 m0, s48
	v_mov_b32_e32 v165, v2
	global_load_lds_dwordx4 v166, s[38:39]
	s_waitcnt vmcnt(8)
	s_waitcnt lgkmcnt(0)
	v_lshl_add_u64 v[188:189], s[38:39], 0, v[164:165]
	v_lshl_add_u64 v[186:187], s[38:39], 0, v[166:167]
	s_barrier
	s_setprio 1
	s_waitcnt lgkmcnt(0)
	v_mfma_f32_16x16x128_f8f6f4 v[96:99], v[20:27], v[198:205], v[96:99]
	v_mfma_f32_16x16x128_f8f6f4 v[92:95], v[28:35], v[198:205], v[92:95]
	v_mfma_f32_16x16x128_f8f6f4 v[80:83], v[20:27], v[226:233], v[80:83]
	v_mfma_f32_16x16x128_f8f6f4 v[76:79], v[28:35], v[226:233], v[76:79]
	v_mfma_f32_16x16x128_f8f6f4 v[64:67], v[20:27], v[234:241], v[64:67]
	v_mfma_f32_16x16x128_f8f6f4 v[60:63], v[28:35], v[234:241], v[60:63]
	v_mfma_f32_16x16x128_f8f6f4 v[48:51], v[20:27], v[242:249], v[48:51]
	v_mfma_f32_16x16x128_f8f6f4 v[44:47], v[28:35], v[242:249], v[44:47]
	s_setprio 0
	s_setprio 1
	v_mfma_f32_16x16x128_f8f6f4 v[88:91], v[4:11], v[198:205], v[88:91]
	v_mfma_f32_16x16x128_f8f6f4 v[84:87], v[12:19], v[198:205], v[84:87]
	v_mfma_f32_16x16x128_f8f6f4 v[72:75], v[4:11], v[226:233], v[72:75]
	v_mfma_f32_16x16x128_f8f6f4 v[68:71], v[12:19], v[226:233], v[68:71]
	v_mfma_f32_16x16x128_f8f6f4 v[56:59], v[4:11], v[234:241], v[56:59]
	v_mfma_f32_16x16x128_f8f6f4 v[52:55], v[12:19], v[234:241], v[52:55]
	v_mfma_f32_16x16x128_f8f6f4 v[40:43], v[4:11], v[242:249], v[40:43]
	v_mfma_f32_16x16x128_f8f6f4 v[36:39], v[12:19], v[242:249], v[36:39]
	s_setprio 0
	s_barrier
	s_add_i32 s66, 0, 0x18000
	s_add_i32 s67, 0, 0x1c000
	ds_read_b128 v[4:7], v192 offset:32768
	ds_read_b128 v[8:11], v207 offset:32768
	ds_read_b128 v[12:15], v192 offset:34816
	ds_read_b128 v[16:19], v207 offset:34816
	ds_read_b128 v[20:23], v192 offset:49152
	ds_read_b128 v[24:27], v207 offset:49152
	ds_read_b128 v[28:31], v192 offset:51200
	ds_read_b128 v[32:35], v207 offset:51200
	v_cndmask_b32_e32 v164, v170, v195, vcc
	v_lshlrev_b32_e32 v165, 10, v164
	v_and_b32_e32 v165, 0x3fffc00, v165
	s_mov_b32 m0, s49
	v_add_u32_e32 v165, v165, v1
	v_bfe_u32 v164, v164, 16, 16
	ds_read_b128 v[198:201], v193 offset:32768
	ds_read_b128 v[202:205], v208 offset:32768
	ds_read_b128 v[226:229], v193 offset:34816
	ds_read_b128 v[230:233], v208 offset:34816
	ds_read_b128 v[234:237], v193 offset:36864
	ds_read_b128 v[238:241], v208 offset:36864
	ds_read_b128 v[242:245], v193 offset:38912
	ds_read_b128 v[246:249], v208 offset:38912
	global_load_lds_dwordx4 v165, s[38:39]
	v_lshl_add_u32 v164, v164, 10, v1
	s_mov_b32 m0, s50
	s_nop 0
	global_load_lds_dwordx4 v164, s[38:39]
	s_waitcnt vmcnt(8)
	s_waitcnt lgkmcnt(0)
	s_barrier
	s_setprio 1
	s_waitcnt lgkmcnt(0)
	v_mfma_f32_16x16x128_f8f6f4 v[160:163], v[4:11], v[198:205], v[160:163]
	v_mfma_f32_16x16x128_f8f6f4 v[156:159], v[12:19], v[198:205], v[156:159]
	v_mfma_f32_16x16x128_f8f6f4 v[144:147], v[4:11], v[226:233], v[144:147]
	v_mfma_f32_16x16x128_f8f6f4 v[140:143], v[12:19], v[226:233], v[140:143]
	v_mfma_f32_16x16x128_f8f6f4 v[128:131], v[4:11], v[234:241], v[128:131]
	v_mfma_f32_16x16x128_f8f6f4 v[124:127], v[12:19], v[234:241], v[124:127]
	v_mfma_f32_16x16x128_f8f6f4 v[112:115], v[4:11], v[242:249], v[112:115]
	v_mfma_f32_16x16x128_f8f6f4 v[108:111], v[12:19], v[242:249], v[108:111]
	s_setprio 0
	s_setprio 1
	v_mfma_f32_16x16x128_f8f6f4 v[152:155], v[20:27], v[198:205], v[152:155]
	v_mfma_f32_16x16x128_f8f6f4 v[148:151], v[28:35], v[198:205], v[148:151]
	v_mfma_f32_16x16x128_f8f6f4 v[136:139], v[20:27], v[226:233], v[136:139]
	v_mfma_f32_16x16x128_f8f6f4 v[132:135], v[28:35], v[226:233], v[132:135]
	v_mfma_f32_16x16x128_f8f6f4 v[120:123], v[20:27], v[234:241], v[120:123]
	v_mfma_f32_16x16x128_f8f6f4 v[116:119], v[28:35], v[234:241], v[116:119]
	v_mfma_f32_16x16x128_f8f6f4 v[104:107], v[20:27], v[242:249], v[104:107]
	v_mfma_f32_16x16x128_f8f6f4 v[100:103], v[28:35], v[242:249], v[100:103]
	s_setprio 0
	s_barrier
	s_add_i32 s38, s66, s46
	v_lshl_add_u64 v[164:165], v[182:183], 0, s[70:71]
	s_mov_b32 m0, s38
	ds_read_b128 v[198:201], v193 offset:49152
	ds_read_b128 v[202:205], v208 offset:49152
	ds_read_b128 v[226:229], v193 offset:51200
	ds_read_b128 v[230:233], v208 offset:51200
	ds_read_b128 v[234:237], v193 offset:53248
	ds_read_b128 v[238:241], v208 offset:53248
	ds_read_b128 v[242:245], v193 offset:55296
	ds_read_b128 v[246:249], v208 offset:55296
	global_load_lds_dwordx4 v[164:165], off
	s_add_i32 m0, s38, 0x2000
	s_add_u32 s36, s36, 0x20080
	v_lshl_add_u64 v[164:165], v[184:185], 0, s[70:71]
	s_addc_u32 s37, s37, 0
	s_add_i32 s38, s67, s46
	global_load_lds_dwordx4 v[164:165], off
	v_lshl_add_u64 v[164:165], s[36:37], 0, v[176:177]
	s_mov_b32 m0, s38
	s_nop 0
	global_load_lds_dwordx4 v[164:165], off
	v_lshl_add_u64 v[164:165], s[36:37], 0, v[174:175]
	s_add_i32 m0, s38, 0x2000
	s_nop 0
	global_load_lds_dwordx4 v[164:165], off
	v_lshl_add_u64 v[164:165], v[188:189], 0, s[70:71]
	s_mov_b32 m0, s55
	s_nop 0
	global_load_lds_dwordx4 v[164:165], off
	v_lshl_add_u64 v[164:165], v[186:187], 0, s[70:71]
	s_mov_b32 m0, s56
	s_nop 0
	global_load_lds_dwordx4 v[164:165], off
	s_waitcnt vmcnt(8)
	s_waitcnt lgkmcnt(0)
	s_barrier
	s_setprio 1
	s_waitcnt lgkmcnt(0)
	v_mfma_f32_16x16x128_f8f6f4 v[96:99], v[4:11], v[198:205], v[96:99]
	v_mfma_f32_16x16x128_f8f6f4 v[92:95], v[12:19], v[198:205], v[92:95]
	v_mfma_f32_16x16x128_f8f6f4 v[80:83], v[4:11], v[226:233], v[80:83]
	v_mfma_f32_16x16x128_f8f6f4 v[76:79], v[12:19], v[226:233], v[76:79]
	v_mfma_f32_16x16x128_f8f6f4 v[64:67], v[4:11], v[234:241], v[64:67]
	v_mfma_f32_16x16x128_f8f6f4 v[60:63], v[12:19], v[234:241], v[60:63]
	v_mfma_f32_16x16x128_f8f6f4 v[48:51], v[4:11], v[242:249], v[48:51]
	v_mfma_f32_16x16x128_f8f6f4 v[44:47], v[12:19], v[242:249], v[44:47]
	s_setprio 0
	s_setprio 1
	v_mfma_f32_16x16x128_f8f6f4 v[88:91], v[20:27], v[198:205], v[88:91]
	v_mfma_f32_16x16x128_f8f6f4 v[84:87], v[28:35], v[198:205], v[84:87]
	v_mfma_f32_16x16x128_f8f6f4 v[72:75], v[20:27], v[226:233], v[72:75]
	v_mfma_f32_16x16x128_f8f6f4 v[68:71], v[28:35], v[226:233], v[68:71]
	v_mfma_f32_16x16x128_f8f6f4 v[56:59], v[20:27], v[234:241], v[56:59]
	v_mfma_f32_16x16x128_f8f6f4 v[52:55], v[28:35], v[234:241], v[52:55]
	v_mfma_f32_16x16x128_f8f6f4 v[40:43], v[20:27], v[242:249], v[40:43]
	v_mfma_f32_16x16x128_f8f6f4 v[36:39], v[28:35], v[242:249], v[36:39]
	s_setprio 0
	s_barrier
	s_add_i32 s65, s65, 2
	s_add_u32 s34, s34, 0x100
	s_addc_u32 s35, s35, 0
	s_add_u32 s63, s63, 0x100
	s_addc_u32 s64, s64, 0
	s_cmp_gt_u32 s65, 5
	s_cbranch_scc0 .LBB0_879
	s_and_b64 vcc, exec, s[26:27]
	s_cbranch_vccz .LBB0_882
	s_barrier

.LBB0_1126:
	s_add_u32 s81, s46, s50
	s_addc_u32 s82, s47, s51
	s_add_u32 s81, s81, 0x100
	s_addc_u32 s82, s82, 0
	s_and_b64 s[54:55], exec, s[54:55]
	s_cselect_b32 s55, s1, s82
	s_cselect_b32 s54, s37, s81
	s_add_i32 s81, 0, 0x10000
	s_add_i32 s82, 0, 0x14000
	ds_read_b128 v[20:23], v205
	ds_read_b128 v[24:27], v250
	ds_read_b128 v[28:31], v205 offset:2048
	ds_read_b128 v[32:35], v250 offset:2048
	ds_read_b128 v[4:7], v205 offset:16384
	ds_read_b128 v[8:11], v250 offset:16384
	ds_read_b128 v[12:15], v205 offset:18432
	ds_read_b128 v[16:19], v250 offset:18432
	v_lshl_add_u64 v[164:165], v[184:185], 0, s[50:51]
	s_add_i32 m0, s65, 0xc000
	ds_read_b128 v[188:191], v206
	ds_read_b128 v[192:195], v255
	ds_read_b128 v[196:199], v206 offset:2048
	ds_read_b128 v[200:203], v255 offset:2048
	ds_read_b128 v[226:229], v206 offset:4096
	ds_read_b128 v[230:233], v255 offset:4096
	ds_read_b128 v[234:237], v206 offset:6144
	ds_read_b128 v[238:241], v255 offset:6144
	global_load_lds_dwordx4 v[164:165], off
	v_lshl_add_u64 v[164:165], v[186:187], 0, s[50:51]
	s_add_i32 m0, s65, 0xe000
	s_nop 0
	global_load_lds_dwordx4 v[164:165], off
	s_waitcnt vmcnt(8)
	s_waitcnt lgkmcnt(0)
	s_barrier
	s_setprio 1
	s_waitcnt lgkmcnt(0)
	v_mfma_f32_16x16x128_f8f6f4 v[160:163], v[20:27], v[188:195], v[160:163]
	v_mfma_f32_16x16x128_f8f6f4 v[156:159], v[28:35], v[188:195], v[156:159]
	v_mfma_f32_16x16x128_f8f6f4 v[144:147], v[20:27], v[196:203], v[144:147]
	v_mfma_f32_16x16x128_f8f6f4 v[140:143], v[28:35], v[196:203], v[140:143]
	v_mfma_f32_16x16x128_f8f6f4 v[128:131], v[20:27], v[226:233], v[128:131]
	v_mfma_f32_16x16x128_f8f6f4 v[124:127], v[28:35], v[226:233], v[124:127]
	v_mfma_f32_16x16x128_f8f6f4 v[112:115], v[20:27], v[234:241], v[112:115]
	v_mfma_f32_16x16x128_f8f6f4 v[108:111], v[28:35], v[234:241], v[108:111]
	s_setprio 0
	s_setprio 1
	v_mfma_f32_16x16x128_f8f6f4 v[152:155], v[4:11], v[188:195], v[152:155]
	v_mfma_f32_16x16x128_f8f6f4 v[148:151], v[12:19], v[188:195], v[148:151]
	v_mfma_f32_16x16x128_f8f6f4 v[136:139], v[4:11], v[196:203], v[136:139]
	v_mfma_f32_16x16x128_f8f6f4 v[132:135], v[12:19], v[196:203], v[132:135]
	v_mfma_f32_16x16x128_f8f6f4 v[120:123], v[4:11], v[226:233], v[120:123]
	v_mfma_f32_16x16x128_f8f6f4 v[116:119], v[12:19], v[226:233], v[116:119]
	v_mfma_f32_16x16x128_f8f6f4 v[104:107], v[4:11], v[234:241], v[104:107]
	v_mfma_f32_16x16x128_f8f6f4 v[100:103], v[12:19], v[234:241], v[100:103]
	s_setprio 0
	s_barrier
	s_add_i32 s81, s81, s62
	v_lshl_add_u64 v[190:191], s[52:53], 0, v[174:175]
	s_mov_b32 m0, s81
	ds_read_b128 v[196:199], v206 offset:16384
	ds_read_b128 v[200:203], v255 offset:16384
	ds_read_b128 v[226:229], v206 offset:18432
	ds_read_b128 v[230:233], v255 offset:18432
	ds_read_b128 v[234:237], v206 offset:20480
	ds_read_b128 v[238:241], v255 offset:20480
	ds_read_b128 v[242:245], v206 offset:22528
	ds_read_b128 v[246:249], v255 offset:22528
	global_load_lds_dwordx4 v[190:191], off
	s_add_i32 m0, s81, 0x2000
	s_add_u32 s84, s52, 0x10000
	v_lshl_add_u64 v[192:193], s[52:53], 0, v[178:179]
	s_addc_u32 s85, s53, 0
	s_add_i32 s81, s82, s62
	global_load_lds_dwordx4 v[192:193], off
	v_lshl_add_u64 v[164:165], s[84:85], 0, v[174:175]
	s_mov_b32 m0, s81
	v_lshl_add_u64 v[194:195], s[54:55], 0, v[172:173]
	global_load_lds_dwordx4 v[164:165], off
	v_lshl_add_u64 v[164:165], s[84:85], 0, v[178:179]
	s_add_i32 m0, s81, 0x2000
	v_lshl_add_u64 v[188:189], s[54:55], 0, v[176:177]
	global_load_lds_dwordx4 v[164:165], off
	s_mov_b32 m0, s65
	s_nop 0
	global_load_lds_dwordx4 v[194:195], off
	s_mov_b32 m0, s66
	s_nop 0
	global_load_lds_dwordx4 v[188:189], off
	s_waitcnt vmcnt(8)
	s_waitcnt lgkmcnt(0)
	s_barrier
	s_setprio 1
	s_waitcnt lgkmcnt(0)
	v_mfma_f32_16x16x128_f8f6f4 v[96:99], v[20:27], v[196:203], v[96:99]
	v_mfma_f32_16x16x128_f8f6f4 v[92:95], v[28:35], v[196:203], v[92:95]
	v_mfma_f32_16x16x128_f8f6f4 v[80:83], v[20:27], v[226:233], v[80:83]
	v_mfma_f32_16x16x128_f8f6f4 v[76:79], v[28:35], v[226:233], v[76:79]
	v_mfma_f32_16x16x128_f8f6f4 v[64:67], v[20:27], v[234:241], v[64:67]
	v_mfma_f32_16x16x128_f8f6f4 v[60:63], v[28:35], v[234:241], v[60:63]
	v_mfma_f32_16x16x128_f8f6f4 v[48:51], v[20:27], v[242:249], v[48:51]
	v_mfma_f32_16x16x128_f8f6f4 v[44:47], v[28:35], v[242:249], v[44:47]
	s_setprio 0
	s_setprio 1
	v_mfma_f32_16x16x128_f8f6f4 v[88:91], v[4:11], v[196:203], v[88:91]
	v_mfma_f32_16x16x128_f8f6f4 v[84:87], v[12:19], v[196:203], v[84:87]
	v_mfma_f32_16x16x128_f8f6f4 v[72:75], v[4:11], v[226:233], v[72:75]
	v_mfma_f32_16x16x128_f8f6f4 v[68:71], v[12:19], v[226:233], v[68:71]
	v_mfma_f32_16x16x128_f8f6f4 v[56:59], v[4:11], v[234:241], v[56:59]
	v_mfma_f32_16x16x128_f8f6f4 v[52:55], v[12:19], v[234:241], v[52:55]
	v_mfma_f32_16x16x128_f8f6f4 v[40:43], v[4:11], v[242:249], v[40:43]
	v_mfma_f32_16x16x128_f8f6f4 v[36:39], v[12:19], v[242:249], v[36:39]
	s_setprio 0
	s_barrier
	s_add_i32 s81, 0, 0x18000
	s_add_i32 s82, 0, 0x1c000
	ds_read_b128 v[4:7], v205 offset:32768
	ds_read_b128 v[8:11], v250 offset:32768
	ds_read_b128 v[12:15], v205 offset:34816
	ds_read_b128 v[16:19], v250 offset:34816
	ds_read_b128 v[20:23], v205 offset:49152
	ds_read_b128 v[24:27], v250 offset:49152
	ds_read_b128 v[28:31], v205 offset:51200
	ds_read_b128 v[32:35], v250 offset:51200
	s_add_u32 s54, s54, 0x20000
	s_addc_u32 s55, s55, 0
	s_mov_b32 m0, s67
	v_lshl_add_u64 v[164:165], s[54:55], 0, v[172:173]
	ds_read_b128 v[196:199], v206 offset:32768
	ds_read_b128 v[200:203], v255 offset:32768
	ds_read_b128 v[226:229], v206 offset:34816
	ds_read_b128 v[230:233], v255 offset:34816
	ds_read_b128 v[234:237], v206 offset:36864
	ds_read_b128 v[238:241], v255 offset:36864
	ds_read_b128 v[242:245], v206 offset:38912
	ds_read_b128 v[246:249], v255 offset:38912
	global_load_lds_dwordx4 v[164:165], off
	v_lshl_add_u64 v[164:165], s[54:55], 0, v[176:177]
	s_mov_b32 m0, s68
	s_nop 0
	global_load_lds_dwordx4 v[164:165], off
	s_waitcnt vmcnt(8)
	s_waitcnt lgkmcnt(0)
	s_barrier
	s_setprio 1
	s_waitcnt lgkmcnt(0)
	v_mfma_f32_16x16x128_f8f6f4 v[160:163], v[4:11], v[196:203], v[160:163]
	v_mfma_f32_16x16x128_f8f6f4 v[156:159], v[12:19], v[196:203], v[156:159]
	v_mfma_f32_16x16x128_f8f6f4 v[144:147], v[4:11], v[226:233], v[144:147]
	v_mfma_f32_16x16x128_f8f6f4 v[140:143], v[12:19], v[226:233], v[140:143]
	v_mfma_f32_16x16x128_f8f6f4 v[128:131], v[4:11], v[234:241], v[128:131]
	v_mfma_f32_16x16x128_f8f6f4 v[124:127], v[12:19], v[234:241], v[124:127]
	v_mfma_f32_16x16x128_f8f6f4 v[112:115], v[4:11], v[242:249], v[112:115]
	v_mfma_f32_16x16x128_f8f6f4 v[108:111], v[12:19], v[242:249], v[108:111]
	s_setprio 0
	s_setprio 1
	v_mfma_f32_16x16x128_f8f6f4 v[152:155], v[20:27], v[196:203], v[152:155]
	v_mfma_f32_16x16x128_f8f6f4 v[148:151], v[28:35], v[196:203], v[148:151]
	v_mfma_f32_16x16x128_f8f6f4 v[136:139], v[20:27], v[226:233], v[136:139]
	v_mfma_f32_16x16x128_f8f6f4 v[132:135], v[28:35], v[226:233], v[132:135]
	v_mfma_f32_16x16x128_f8f6f4 v[120:123], v[20:27], v[234:241], v[120:123]
	v_mfma_f32_16x16x128_f8f6f4 v[116:119], v[28:35], v[234:241], v[116:119]
	v_mfma_f32_16x16x128_f8f6f4 v[104:107], v[20:27], v[242:249], v[104:107]
	v_mfma_f32_16x16x128_f8f6f4 v[100:103], v[28:35], v[242:249], v[100:103]
	s_setprio 0
	s_barrier
	s_mov_b64 s[84:85], 0x80
	s_add_i32 s54, s81, s62
	v_lshl_add_u64 v[164:165], v[190:191], 0, s[84:85]
	s_mov_b32 m0, s54
	ds_read_b128 v[196:199], v206 offset:49152
	ds_read_b128 v[200:203], v255 offset:49152
	ds_read_b128 v[226:229], v206 offset:51200
	ds_read_b128 v[230:233], v255 offset:51200
	ds_read_b128 v[234:237], v206 offset:53248
	ds_read_b128 v[238:241], v255 offset:53248
	ds_read_b128 v[242:245], v206 offset:55296
	ds_read_b128 v[246:249], v255 offset:55296
	global_load_lds_dwordx4 v[164:165], off
	s_add_i32 m0, s54, 0x2000
	s_add_u32 s52, s52, 0x10080
	v_lshl_add_u64 v[164:165], v[192:193], 0, s[84:85]
	s_addc_u32 s53, s53, 0
	s_add_i32 s54, s82, s62
	global_load_lds_dwordx4 v[164:165], off
	v_lshl_add_u64 v[164:165], s[52:53], 0, v[174:175]
	s_mov_b32 m0, s54
	s_nop 0
	global_load_lds_dwordx4 v[164:165], off
	v_lshl_add_u64 v[164:165], s[52:53], 0, v[178:179]
	s_add_i32 m0, s54, 0x2000
	s_nop 0
	global_load_lds_dwordx4 v[164:165], off
	v_lshl_add_u64 v[164:165], v[194:195], 0, s[84:85]
	s_mov_b32 m0, s71
	s_nop 0
	global_load_lds_dwordx4 v[164:165], off
	v_lshl_add_u64 v[164:165], v[188:189], 0, s[84:85]
	s_mov_b32 m0, s72
	s_nop 0
	global_load_lds_dwordx4 v[164:165], off
	s_waitcnt vmcnt(8)
	s_waitcnt lgkmcnt(0)
	s_barrier
	s_setprio 1
	s_waitcnt lgkmcnt(0)
	v_mfma_f32_16x16x128_f8f6f4 v[96:99], v[4:11], v[196:203], v[96:99]
	v_mfma_f32_16x16x128_f8f6f4 v[92:95], v[12:19], v[196:203], v[92:95]
	v_mfma_f32_16x16x128_f8f6f4 v[80:83], v[4:11], v[226:233], v[80:83]
	v_mfma_f32_16x16x128_f8f6f4 v[76:79], v[12:19], v[226:233], v[76:79]
	v_mfma_f32_16x16x128_f8f6f4 v[64:67], v[4:11], v[234:241], v[64:67]
	v_mfma_f32_16x16x128_f8f6f4 v[60:63], v[12:19], v[234:241], v[60:63]
	v_mfma_f32_16x16x128_f8f6f4 v[48:51], v[4:11], v[242:249], v[48:51]
	v_mfma_f32_16x16x128_f8f6f4 v[44:47], v[12:19], v[242:249], v[44:47]
	s_setprio 0
	s_setprio 1
	v_mfma_f32_16x16x128_f8f6f4 v[88:91], v[20:27], v[196:203], v[88:91]
	v_mfma_f32_16x16x128_f8f6f4 v[84:87], v[28:35], v[196:203], v[84:87]
	v_mfma_f32_16x16x128_f8f6f4 v[72:75], v[20:27], v[226:233], v[72:75]
	v_mfma_f32_16x16x128_f8f6f4 v[68:71], v[28:35], v[226:233], v[68:71]
	v_mfma_f32_16x16x128_f8f6f4 v[56:59], v[20:27], v[234:241], v[56:59]
	v_mfma_f32_16x16x128_f8f6f4 v[52:55], v[28:35], v[234:241], v[52:55]
	v_mfma_f32_16x16x128_f8f6f4 v[40:43], v[20:27], v[242:249], v[40:43]
	v_mfma_f32_16x16x128_f8f6f4 v[36:39], v[28:35], v[242:249], v[36:39]
	s_setprio 0
	s_barrier
	s_add_u32 s50, s50, 0x100
	s_mov_b64 s[52:53], s[88:89]
	s_addc_u32 s51, s51, 0
	s_add_i32 s52, s52, 2
	s_cmp_gt_u32 s52, 5
	s_cbranch_scc1 .LBB0_1129
